# v5 + P10 setup: the 20 row-table loads issued as one batch (zero-address select instead of data select removes the vmcnt(0) after every load)
# baseline (speedup 1.0000x reference)
.LBB0_1064:
	v_mov_b32_e32 v254, s82
	v_mov_b32_e32 v255, s83
	s_andn2_b64 vcc, exec, s[4:5]
	s_cbranch_vccnz .LBB0_1066
	s_lshl_b32 s4, s20, 2
	s_add_i32 s5, 0, 0x20000
	s_add_i32 s4, s5, s4
	v_mov_b32_e32 v1, s4
	ds_read_b32 v1, v1 offset:132
	s_waitcnt lgkmcnt(0)
	v_lshlrev_b32_e32 v2, 2, v1
	v_add_u32_e32 v2, s5, v2
	ds_read_b32 v3, v2
	ds_read_b32 v4, v2 offset:1440
	s_waitcnt lgkmcnt(1)
	v_sub_u32_e32 v2, s20, v3
	v_lshl_or_b32 v5, v2, 8, v0
	v_lshl_add_u32 v2, v1, 14, v5
	v_ashrrev_i32_e32 v3, 31, v2
	v_lshl_add_u64 v[2:3], v[2:3], 2, s[2:3]
	s_waitcnt lgkmcnt(0)
	v_cmp_lt_i32_e32 vcc, v5, v4
	v_cmp_lt_i32_e64 s[4:5], -1, v4
	s_nop 1
	v_cndmask_b32_e32 v2, v254, v2, vcc
	v_cndmask_b32_e32 v3, v255, v3, vcc
	global_load_dword v1, v[2:3], off
	s_branch .LBB0_1067

.LBB0_1071:
	s_andn2_b64 vcc, exec, s[12:13]
	s_cbranch_vccnz .LBB0_1073
	s_lshl_b32 s6, s20, 2
	s_add_i32 s7, 0, 0x20000
	s_add_i32 s6, s7, s6
	v_mov_b32_e32 v2, s6
	ds_read_b32 v2, v2 offset:132
	s_waitcnt lgkmcnt(0)
	v_lshlrev_b32_e32 v3, 2, v2
	v_add_u32_e32 v3, s7, v3
	ds_read_b32 v4, v3
	ds_read_b32 v5, v3 offset:1440
	s_waitcnt lgkmcnt(1)
	v_sub_u32_e32 v3, s20, v4
	v_lshl_or_b32 v4, v3, 8, v0
	v_lshl_add_u32 v2, v2, 14, v4
	v_ashrrev_i32_e32 v3, 31, v2
	v_lshl_add_u64 v[2:3], v[2:3], 2, s[2:3]
	s_waitcnt lgkmcnt(0)
	v_cmp_lt_i32_e32 vcc, v4, v5
	v_cmp_lt_i32_e64 s[6:7], -1, v5
	s_nop 1
	v_cndmask_b32_e32 v2, v254, v2, vcc
	v_cndmask_b32_e32 v3, v255, v3, vcc
	global_load_dword v2, v[2:3], off
	s_branch .LBB0_1074

.LBB0_1078:
	s_andn2_b64 vcc, exec, s[12:13]
	s_cbranch_vccnz .LBB0_1080
	s_add_i32 s12, 0, 0x20000
	v_lshl_add_u32 v3, v11, 2, s12
	ds_read_b32 v3, v3 offset:132
	s_waitcnt lgkmcnt(0)
	v_lshl_add_u32 v4, v3, 2, s12
	ds_read_b32 v5, v4
	ds_read_b32 v6, v4 offset:1440
	s_waitcnt lgkmcnt(1)
	v_sub_u32_e32 v4, v11, v5
	v_lshl_or_b32 v7, v4, 8, v0
	v_lshl_add_u32 v4, v3, 14, v7
	v_ashrrev_i32_e32 v5, 31, v4
	v_lshl_add_u64 v[4:5], v[4:5], 2, s[2:3]
	s_waitcnt lgkmcnt(0)
	v_cmp_lt_i32_e32 vcc, -1, v6
	v_cmp_lt_i32_e64 s[12:13], v7, v6
	s_nop 1
	v_cndmask_b32_e64 v4, v254, v4, s[12:13]
	v_cndmask_b32_e64 v5, v255, v5, s[12:13]
	global_load_dword v3, v[4:5], off
	s_and_b64 s[12:13], vcc, exec
	s_branch .LBB0_1081

.LBB0_1085:
	s_andn2_b64 vcc, exec, s[12:13]
	s_cbranch_vccnz .LBB0_1087
	s_add_i32 s12, 0, 0x20000
	v_lshl_add_u32 v4, v11, 2, s12
	ds_read_b32 v4, v4 offset:132
	s_waitcnt lgkmcnt(0)
	v_lshl_add_u32 v5, v4, 2, s12
	ds_read_b32 v6, v5
	ds_read_b32 v7, v5 offset:1440
	s_waitcnt lgkmcnt(1)
	v_sub_u32_e32 v5, v11, v6
	v_lshl_or_b32 v6, v5, 8, v0
	v_lshl_add_u32 v4, v4, 14, v6
	v_ashrrev_i32_e32 v5, 31, v4
	v_lshl_add_u64 v[4:5], v[4:5], 2, s[2:3]
	s_waitcnt lgkmcnt(0)
	v_cmp_lt_i32_e32 vcc, -1, v7
	v_cmp_lt_i32_e64 s[12:13], v6, v7
	s_nop 1
	v_cndmask_b32_e64 v4, v254, v4, s[12:13]
	v_cndmask_b32_e64 v5, v255, v5, s[12:13]
	global_load_dword v4, v[4:5], off
	s_and_b64 s[12:13], vcc, exec
	s_branch .LBB0_1088

.LBB0_1092:
	s_andn2_b64 vcc, exec, s[12:13]
	s_cbranch_vccnz .LBB0_1094
	s_add_i32 s12, 0, 0x20000
	v_lshl_add_u32 v5, v11, 2, s12
	ds_read_b32 v5, v5 offset:132
	s_waitcnt lgkmcnt(0)
	v_lshl_add_u32 v6, v5, 2, s12
	ds_read_b32 v7, v6
	ds_read_b32 v8, v6 offset:1440
	s_waitcnt lgkmcnt(1)
	v_sub_u32_e32 v6, v11, v7
	v_lshl_or_b32 v9, v6, 8, v0
	v_lshl_add_u32 v6, v5, 14, v9
	v_ashrrev_i32_e32 v7, 31, v6
	v_lshl_add_u64 v[6:7], v[6:7], 2, s[2:3]
	s_waitcnt lgkmcnt(0)
	v_cmp_lt_i32_e32 vcc, -1, v8
	v_cmp_lt_i32_e64 s[12:13], v9, v8
	s_nop 1
	v_cndmask_b32_e64 v6, v254, v6, s[12:13]
	v_cndmask_b32_e64 v7, v255, v7, s[12:13]
	global_load_dword v5, v[6:7], off
	s_and_b64 s[12:13], vcc, exec
	s_branch .LBB0_1095

.LBB0_1099:
	s_andn2_b64 vcc, exec, s[12:13]
	s_cbranch_vccnz .LBB0_1101
	s_add_i32 s12, 0, 0x20000
	v_lshl_add_u32 v6, v11, 2, s12
	ds_read_b32 v6, v6 offset:132
	s_waitcnt lgkmcnt(0)
	v_lshl_add_u32 v7, v6, 2, s12
	ds_read_b32 v8, v7
	ds_read_b32 v9, v7 offset:1440
	s_waitcnt lgkmcnt(1)
	v_sub_u32_e32 v7, v11, v8
	v_lshl_or_b32 v8, v7, 8, v0
	v_lshl_add_u32 v6, v6, 14, v8
	v_ashrrev_i32_e32 v7, 31, v6
	v_lshl_add_u64 v[6:7], v[6:7], 2, s[2:3]
	s_waitcnt lgkmcnt(0)
	v_cmp_lt_i32_e32 vcc, -1, v9
	v_cmp_lt_i32_e64 s[12:13], v8, v9
	s_nop 1
	v_cndmask_b32_e64 v6, v254, v6, s[12:13]
	v_cndmask_b32_e64 v7, v255, v7, s[12:13]
	global_load_dword v6, v[6:7], off
	s_and_b64 s[12:13], vcc, exec
	s_branch .LBB0_1102

.LBB0_1106:
	s_andn2_b64 vcc, exec, s[12:13]
	s_cbranch_vccnz .LBB0_1108
	s_add_i32 s12, 0, 0x20000
	v_lshl_add_u32 v7, v11, 2, s12
	ds_read_b32 v7, v7 offset:132
	s_waitcnt lgkmcnt(0)
	v_lshl_add_u32 v8, v7, 2, s12
	ds_read_b32 v9, v8
	ds_read_b32 v10, v8 offset:1440
	s_waitcnt lgkmcnt(1)
	v_sub_u32_e32 v8, v11, v9
	v_lshl_or_b32 v12, v8, 8, v0
	v_lshl_add_u32 v8, v7, 14, v12
	v_ashrrev_i32_e32 v9, 31, v8
	v_lshl_add_u64 v[8:9], v[8:9], 2, s[2:3]
	s_waitcnt lgkmcnt(0)
	v_cmp_lt_i32_e32 vcc, -1, v10
	v_cmp_lt_i32_e64 s[12:13], v12, v10
	s_nop 1
	v_cndmask_b32_e64 v8, v254, v8, s[12:13]
	v_cndmask_b32_e64 v9, v255, v9, s[12:13]
	global_load_dword v7, v[8:9], off
	s_and_b64 s[12:13], vcc, exec
	s_branch .LBB0_1109

.LBB0_1113:
	s_andn2_b64 vcc, exec, s[12:13]
	s_cbranch_vccnz .LBB0_1115
	s_add_i32 s12, 0, 0x20000
	v_lshl_add_u32 v8, v11, 2, s12
	ds_read_b32 v8, v8 offset:132
	s_waitcnt lgkmcnt(0)
	v_lshl_add_u32 v9, v8, 2, s12
	ds_read_b32 v10, v9
	ds_read_b32 v12, v9 offset:1440
	s_waitcnt lgkmcnt(1)
	v_sub_u32_e32 v9, v11, v10
	v_lshl_or_b32 v10, v9, 8, v0
	v_lshl_add_u32 v8, v8, 14, v10
	v_ashrrev_i32_e32 v9, 31, v8
	v_lshl_add_u64 v[8:9], v[8:9], 2, s[2:3]
	s_waitcnt lgkmcnt(0)
	v_cmp_lt_i32_e32 vcc, -1, v12
	v_cmp_lt_i32_e64 s[12:13], v10, v12
	s_nop 1
	v_cndmask_b32_e64 v8, v254, v8, s[12:13]
	v_cndmask_b32_e64 v9, v255, v9, s[12:13]
	global_load_dword v8, v[8:9], off
	s_and_b64 s[12:13], vcc, exec
	s_branch .LBB0_1116

.LBB0_1120:
	s_andn2_b64 vcc, exec, s[12:13]
	s_cbranch_vccnz .LBB0_1122
	s_add_i32 s12, 0, 0x20000
	v_lshl_add_u32 v9, v11, 2, s12
	ds_read_b32 v9, v9 offset:132
	s_waitcnt lgkmcnt(0)
	v_lshl_add_u32 v10, v9, 2, s12
	ds_read_b32 v12, v10
	ds_read_b32 v10, v10 offset:1440
	s_waitcnt lgkmcnt(1)
	v_sub_u32_e32 v12, v11, v12
	v_lshl_or_b32 v14, v12, 8, v0
	v_lshl_add_u32 v12, v9, 14, v14
	v_ashrrev_i32_e32 v13, 31, v12
	v_lshl_add_u64 v[12:13], v[12:13], 2, s[2:3]
	s_waitcnt lgkmcnt(0)
	v_cmp_lt_i32_e32 vcc, -1, v10
	v_cmp_lt_i32_e64 s[12:13], v14, v10
	s_nop 1
	v_cndmask_b32_e64 v12, v254, v12, s[12:13]
	v_cndmask_b32_e64 v13, v255, v13, s[12:13]
	global_load_dword v9, v[12:13], off
	s_and_b64 s[12:13], vcc, exec
	s_branch .LBB0_1123

.LBB0_1127:
	s_andn2_b64 vcc, exec, s[12:13]
	s_cbranch_vccnz .LBB0_1129
	s_add_i32 s12, 0, 0x20000
	v_lshl_add_u32 v10, v11, 2, s12
	ds_read_b32 v10, v10 offset:132
	s_waitcnt lgkmcnt(0)
	v_lshl_add_u32 v12, v10, 2, s12
	ds_read_b32 v13, v12
	ds_read_b32 v14, v12 offset:1440
	s_waitcnt lgkmcnt(1)
	v_sub_u32_e32 v12, v11, v13
	v_lshl_or_b32 v15, v12, 8, v0
	v_lshl_add_u32 v12, v10, 14, v15
	v_ashrrev_i32_e32 v13, 31, v12
	v_lshl_add_u64 v[12:13], v[12:13], 2, s[2:3]
	s_waitcnt lgkmcnt(0)
	v_cmp_lt_i32_e32 vcc, -1, v14
	v_cmp_lt_i32_e64 s[12:13], v15, v14
	s_nop 1
	v_cndmask_b32_e64 v12, v254, v12, s[12:13]
	v_cndmask_b32_e64 v13, v255, v13, s[12:13]
	global_load_dword v10, v[12:13], off
	s_and_b64 s[12:13], vcc, exec
	s_branch .LBB0_1130

.LBB0_1134:
	s_andn2_b64 vcc, exec, s[12:13]
	s_cbranch_vccnz .LBB0_1136
	s_add_i32 s12, 0, 0x20000
	v_lshl_add_u32 v12, v11, 2, s12
	ds_read_b32 v12, v12 offset:132
	s_waitcnt lgkmcnt(0)
	v_lshl_add_u32 v13, v12, 2, s12
	ds_read_b32 v14, v13
	ds_read_b32 v15, v13 offset:1440
	s_waitcnt lgkmcnt(1)
	v_sub_u32_e32 v13, v11, v14
	v_lshl_or_b32 v14, v13, 8, v0
	v_lshl_add_u32 v12, v12, 14, v14
	v_ashrrev_i32_e32 v13, 31, v12
	v_lshl_add_u64 v[12:13], v[12:13], 2, s[2:3]
	s_waitcnt lgkmcnt(0)
	v_cmp_lt_i32_e32 vcc, -1, v15
	v_cmp_lt_i32_e64 s[12:13], v14, v15
	s_nop 1
	v_cndmask_b32_e64 v12, v254, v12, s[12:13]
	v_cndmask_b32_e64 v13, v255, v13, s[12:13]
	global_load_dword v12, v[12:13], off
	s_and_b64 s[12:13], vcc, exec
	s_branch .LBB0_1137

.LBB0_1141:
	s_andn2_b64 vcc, exec, s[12:13]
	s_cbranch_vccnz .LBB0_1143
	s_add_i32 s12, 0, 0x20000
	v_lshl_add_u32 v13, v11, 2, s12
	ds_read_b32 v13, v13 offset:132
	s_waitcnt lgkmcnt(0)
	v_lshl_add_u32 v14, v13, 2, s12
	ds_read_b32 v15, v14
	ds_read_b32 v16, v14 offset:1440
	s_waitcnt lgkmcnt(1)
	v_sub_u32_e32 v14, v11, v15
	v_lshl_or_b32 v17, v14, 8, v0
	v_lshl_add_u32 v14, v13, 14, v17
	v_ashrrev_i32_e32 v15, 31, v14
	v_lshl_add_u64 v[14:15], v[14:15], 2, s[2:3]
	s_waitcnt lgkmcnt(0)
	v_cmp_lt_i32_e32 vcc, -1, v16
	v_cmp_lt_i32_e64 s[12:13], v17, v16
	s_nop 1
	v_cndmask_b32_e64 v14, v254, v14, s[12:13]
	v_cndmask_b32_e64 v15, v255, v15, s[12:13]
	global_load_dword v13, v[14:15], off
	s_and_b64 s[12:13], vcc, exec
	s_branch .LBB0_1144

.LBB0_1148:
	s_andn2_b64 vcc, exec, s[12:13]
	s_cbranch_vccnz .LBB0_1150
	s_add_i32 s12, 0, 0x20000
	v_lshl_add_u32 v14, v11, 2, s12
	ds_read_b32 v14, v14 offset:132
	s_waitcnt lgkmcnt(0)
	v_lshl_add_u32 v15, v14, 2, s12
	ds_read_b32 v16, v15
	ds_read_b32 v17, v15 offset:1440
	s_waitcnt lgkmcnt(1)
	v_sub_u32_e32 v15, v11, v16
	v_lshl_or_b32 v16, v15, 8, v0
	v_lshl_add_u32 v14, v14, 14, v16
	v_ashrrev_i32_e32 v15, 31, v14
	v_lshl_add_u64 v[14:15], v[14:15], 2, s[2:3]
	s_waitcnt lgkmcnt(0)
	v_cmp_lt_i32_e32 vcc, -1, v17
	v_cmp_lt_i32_e64 s[12:13], v16, v17
	s_nop 1
	v_cndmask_b32_e64 v14, v254, v14, s[12:13]
	v_cndmask_b32_e64 v15, v255, v15, s[12:13]
	global_load_dword v14, v[14:15], off
	s_and_b64 s[12:13], vcc, exec
	s_branch .LBB0_1151

.LBB0_1155:
	s_andn2_b64 vcc, exec, s[12:13]
	s_cbranch_vccnz .LBB0_1157
	s_add_i32 s12, 0, 0x20000
	v_lshl_add_u32 v15, v11, 2, s12
	ds_read_b32 v15, v15 offset:132
	s_waitcnt lgkmcnt(0)
	v_lshl_add_u32 v16, v15, 2, s12
	ds_read_b32 v17, v16
	ds_read_b32 v18, v16 offset:1440
	s_waitcnt lgkmcnt(1)
	v_sub_u32_e32 v16, v11, v17
	v_lshl_or_b32 v19, v16, 8, v0
	v_lshl_add_u32 v16, v15, 14, v19
	v_ashrrev_i32_e32 v17, 31, v16
	v_lshl_add_u64 v[16:17], v[16:17], 2, s[2:3]
	s_waitcnt lgkmcnt(0)
	v_cmp_lt_i32_e32 vcc, -1, v18
	v_cmp_lt_i32_e64 s[12:13], v19, v18
	s_nop 1
	v_cndmask_b32_e64 v16, v254, v16, s[12:13]
	v_cndmask_b32_e64 v17, v255, v17, s[12:13]
	global_load_dword v15, v[16:17], off
	s_and_b64 s[12:13], vcc, exec
	s_branch .LBB0_1158

.LBB0_1162:
	s_andn2_b64 vcc, exec, s[12:13]
	s_cbranch_vccnz .LBB0_1164
	s_add_i32 s12, 0, 0x20000
	v_lshl_add_u32 v16, v11, 2, s12
	ds_read_b32 v16, v16 offset:132
	s_waitcnt lgkmcnt(0)
	v_lshl_add_u32 v17, v16, 2, s12
	ds_read_b32 v18, v17
	ds_read_b32 v19, v17 offset:1440
	s_waitcnt lgkmcnt(1)
	v_sub_u32_e32 v17, v11, v18
	v_lshl_or_b32 v18, v17, 8, v0
	v_lshl_add_u32 v16, v16, 14, v18
	v_ashrrev_i32_e32 v17, 31, v16
	v_lshl_add_u64 v[16:17], v[16:17], 2, s[2:3]
	s_waitcnt lgkmcnt(0)
	v_cmp_lt_i32_e32 vcc, -1, v19
	v_cmp_lt_i32_e64 s[12:13], v18, v19
	s_nop 1
	v_cndmask_b32_e64 v16, v254, v16, s[12:13]
	v_cndmask_b32_e64 v17, v255, v17, s[12:13]
	global_load_dword v16, v[16:17], off
	s_and_b64 s[12:13], vcc, exec
	s_branch .LBB0_1165

.LBB0_1169:
	s_andn2_b64 vcc, exec, s[12:13]
	s_cbranch_vccnz .LBB0_1171
	s_add_i32 s12, 0, 0x20000
	v_lshl_add_u32 v17, v11, 2, s12
	ds_read_b32 v17, v17 offset:132
	s_waitcnt lgkmcnt(0)
	v_lshl_add_u32 v18, v17, 2, s12
	ds_read_b32 v19, v18
	ds_read_b32 v20, v18 offset:1440
	s_waitcnt lgkmcnt(1)
	v_sub_u32_e32 v18, v11, v19
	v_lshl_or_b32 v21, v18, 8, v0
	v_lshl_add_u32 v18, v17, 14, v21
	v_ashrrev_i32_e32 v19, 31, v18
	v_lshl_add_u64 v[18:19], v[18:19], 2, s[2:3]
	s_waitcnt lgkmcnt(0)
	v_cmp_lt_i32_e32 vcc, -1, v20
	v_cmp_lt_i32_e64 s[12:13], v21, v20
	s_nop 1
	v_cndmask_b32_e64 v18, v254, v18, s[12:13]
	v_cndmask_b32_e64 v19, v255, v19, s[12:13]
	global_load_dword v17, v[18:19], off
	s_and_b64 s[12:13], vcc, exec
	s_branch .LBB0_1172

.LBB0_1176:
	s_andn2_b64 vcc, exec, s[12:13]
	s_cbranch_vccnz .LBB0_1178
	s_add_i32 s12, 0, 0x20000
	v_lshl_add_u32 v18, v11, 2, s12
	ds_read_b32 v18, v18 offset:132
	s_waitcnt lgkmcnt(0)
	v_lshl_add_u32 v19, v18, 2, s12
	ds_read_b32 v20, v19
	ds_read_b32 v21, v19 offset:1440
	s_waitcnt lgkmcnt(1)
	v_sub_u32_e32 v19, v11, v20
	v_lshl_or_b32 v20, v19, 8, v0
	v_lshl_add_u32 v18, v18, 14, v20
	v_ashrrev_i32_e32 v19, 31, v18
	v_lshl_add_u64 v[18:19], v[18:19], 2, s[2:3]
	s_waitcnt lgkmcnt(0)
	v_cmp_lt_i32_e32 vcc, -1, v21
	v_cmp_lt_i32_e64 s[12:13], v20, v21
	s_nop 1
	v_cndmask_b32_e64 v18, v254, v18, s[12:13]
	v_cndmask_b32_e64 v19, v255, v19, s[12:13]
	global_load_dword v18, v[18:19], off
	s_and_b64 s[12:13], vcc, exec
	s_branch .LBB0_1179

.LBB0_1183:
	s_andn2_b64 vcc, exec, s[12:13]
	s_cbranch_vccnz .LBB0_1185
	s_add_i32 s12, 0, 0x20000
	v_lshl_add_u32 v19, v11, 2, s12
	ds_read_b32 v19, v19 offset:132
	s_waitcnt lgkmcnt(0)
	v_lshl_add_u32 v20, v19, 2, s12
	ds_read_b32 v21, v20
	ds_read_b32 v22, v20 offset:1440
	s_waitcnt lgkmcnt(1)
	v_sub_u32_e32 v11, v11, v21
	v_lshl_or_b32 v11, v11, 8, v0
	v_lshl_add_u32 v20, v19, 14, v11
	v_ashrrev_i32_e32 v21, 31, v20
	v_lshl_add_u64 v[20:21], v[20:21], 2, s[2:3]
	s_waitcnt lgkmcnt(0)
	v_cmp_lt_i32_e32 vcc, -1, v22
	v_cmp_lt_i32_e64 s[12:13], v11, v22
	s_nop 1
	v_cndmask_b32_e64 v20, v254, v20, s[12:13]
	v_cndmask_b32_e64 v21, v255, v21, s[12:13]
	global_load_dword v19, v[20:21], off
	s_and_b64 s[12:13], vcc, exec
	s_branch .LBB0_1186

.LBB0_1187:
	s_or_b64 exec, exec, s[50:51]
	v_mov_b32_e32 v20, 0
	s_mov_b64 s[50:51], 0
	s_mov_b64 s[52:53], 0
	v_mov_b32_e32 v21, 0
	s_and_saveexec_b64 s[54:55], s[10:11]
	s_cbranch_execz .LBB0_1192
	s_mul_i32 s52, s80, 18
	s_mul_hi_i32 s53, s80, 18
	s_add_u32 s52, s52, s90
	s_addc_u32 s53, s53, s56
	v_mov_b64_e32 v[22:23], s[0:1]
	v_cmp_ge_i64_e32 vcc, s[52:53], v[22:23]
	s_cbranch_vccnz .LBB0_1190
	s_ashr_i32 s53, s52, 31
	s_lshr_b32 s53, s53, 29
	s_add_i32 s53, s52, s53
	s_ashr_i32 s57, s53, 3
	s_and_b32 s53, s53, -8
	s_sub_i32 s52, s52, s53
	v_mov_b32_e32 v11, s52
	v_alignbit_b32 v11, s33, v11, 31
	s_nop 0
	v_readfirstlane_b32 s53, v11
	s_mul_i32 s52, s53, s52
	s_add_i32 s52, s52, s57
	s_ashr_i32 s53, s52, 31
	s_lshr_b32 s53, s53, 26
	s_add_i32 s53, s52, s53
	s_ashr_i32 s57, s53, 6
	s_lshl_b32 s57, s57, 2
	s_sub_i32 s58, s33, s57
	s_min_i32 s58, s58, 4
	s_abs_i32 s58, s58
	v_cvt_f32_u32_e32 v11, s58
	s_sub_i32 s59, 0, s58
	s_andn2_b32 s53, s53, 63
	s_sub_i32 s52, s52, s53
	v_rcp_iflag_f32_e32 v11, v11
	s_ashr_i32 s53, s52, 31
	s_abs_i32 s52, s52
	v_mul_f32_e32 v11, 0x4f7ffffe, v11
	v_cvt_u32_f32_e32 v11, v11
	s_nop 0
	v_readfirstlane_b32 s60, v11
	s_mul_i32 s59, s59, s60
	s_mul_hi_u32 s59, s60, s59
	s_add_i32 s60, s60, s59
	s_mul_hi_u32 s59, s52, s60
	s_mul_i32 s59, s59, s58
	s_sub_i32 s52, s52, s59
	s_sub_i32 s59, s52, s58
	s_cmp_ge_u32 s52, s58
	s_cselect_b32 s52, s59, s52
	s_sub_i32 s59, s52, s58
	s_cmp_ge_u32 s52, s58
	s_cselect_b32 s52, s59, s52
	s_xor_b32 s52, s52, s53
	s_sub_i32 s52, s52, s53
	s_add_i32 s52, s52, s57
	s_lshl_b32 s53, s52, 2
	s_add_i32 s57, 0, 0x20000
	s_add_i32 s53, s57, s53
	v_mov_b32_e32 v11, s53
	ds_read_b32 v11, v11 offset:132
	s_waitcnt lgkmcnt(0)
	v_lshlrev_b32_e32 v21, 2, v11
	v_add_u32_e32 v21, s57, v21
	ds_read_b32 v22, v21
	ds_read_b32 v21, v21 offset:1440
	s_waitcnt lgkmcnt(1)
	v_sub_u32_e32 v22, s52, v22
	v_lshl_or_b32 v24, v22, 8, v0
	v_lshl_add_u32 v22, v11, 14, v24
	v_ashrrev_i32_e32 v23, 31, v22
	v_lshl_add_u64 v[22:23], v[22:23], 2, s[2:3]
	s_waitcnt lgkmcnt(0)
	v_cmp_lt_i32_e32 vcc, v24, v21
	v_cmp_lt_i32_e64 s[52:53], -1, v21
	s_nop 1
	v_cndmask_b32_e32 v22, v254, v22, vcc
	v_cndmask_b32_e32 v23, v255, v23, vcc
	global_load_dword v21, v[22:23], off
	s_branch .LBB0_1191

.LBB0_1192:
	s_or_b64 exec, exec, s[54:55]
	s_and_saveexec_b64 s[54:55], s[10:11]
	s_cbranch_execz .LBB0_1197
	s_mul_i32 s50, s80, 19
	s_mul_hi_i32 s51, s80, 19
	s_add_u32 s50, s50, s90
	s_addc_u32 s51, s51, s56
	v_mov_b64_e32 v[22:23], s[0:1]
	v_cmp_ge_i64_e32 vcc, s[50:51], v[22:23]
	s_cbranch_vccnz .LBB0_1195
	s_ashr_i32 s51, s50, 31
	s_lshr_b32 s51, s51, 29
	s_add_i32 s51, s50, s51
	s_ashr_i32 s57, s51, 3
	s_and_b32 s51, s51, -8
	s_sub_i32 s50, s50, s51
	v_mov_b32_e32 v11, s50
	v_alignbit_b32 v11, s33, v11, 31
	s_nop 0
	v_readfirstlane_b32 s51, v11
	s_mul_i32 s50, s51, s50
	s_add_i32 s50, s50, s57
	s_ashr_i32 s51, s50, 31
	s_lshr_b32 s51, s51, 26
	s_add_i32 s51, s50, s51
	s_ashr_i32 s57, s51, 6
	s_lshl_b32 s57, s57, 2
	s_sub_i32 s58, s33, s57
	s_min_i32 s58, s58, 4
	s_abs_i32 s58, s58
	v_cvt_f32_u32_e32 v11, s58
	s_sub_i32 s59, 0, s58
	s_andn2_b32 s51, s51, 63
	s_sub_i32 s50, s50, s51
	v_rcp_iflag_f32_e32 v11, v11
	s_ashr_i32 s51, s50, 31
	s_abs_i32 s50, s50
	v_mul_f32_e32 v11, 0x4f7ffffe, v11
	v_cvt_u32_f32_e32 v11, v11
	s_nop 0
	v_readfirstlane_b32 s60, v11
	s_mul_i32 s59, s59, s60
	s_mul_hi_u32 s59, s60, s59
	s_add_i32 s60, s60, s59
	s_mul_hi_u32 s59, s50, s60
	s_mul_i32 s59, s59, s58
	s_sub_i32 s50, s50, s59
	s_sub_i32 s59, s50, s58
	s_cmp_ge_u32 s50, s58
	s_cselect_b32 s50, s59, s50
	s_sub_i32 s59, s50, s58
	s_cmp_ge_u32 s50, s58
	s_cselect_b32 s50, s59, s50
	s_xor_b32 s50, s50, s51
	s_sub_i32 s50, s50, s51
	s_add_i32 s50, s50, s57
	s_lshl_b32 s51, s50, 2
	s_add_i32 s57, 0, 0x20000
	s_add_i32 s51, s57, s51
	v_mov_b32_e32 v11, s51
	ds_read_b32 v11, v11 offset:132
	s_waitcnt lgkmcnt(0)
	v_lshlrev_b32_e32 v20, 2, v11
	v_add_u32_e32 v20, s57, v20
	ds_read_b32 v22, v20
	ds_read_b32 v20, v20 offset:1440
	s_waitcnt lgkmcnt(1)
	v_sub_u32_e32 v22, s50, v22
	v_lshl_or_b32 v24, v22, 8, v0
	v_lshl_add_u32 v22, v11, 14, v24
	v_ashrrev_i32_e32 v23, 31, v22
	v_lshl_add_u64 v[22:23], v[22:23], 2, s[2:3]
	s_waitcnt lgkmcnt(0)
	v_cmp_lt_i32_e32 vcc, v24, v20
	v_cmp_lt_i32_e64 s[50:51], -1, v20
	s_nop 1
	v_cndmask_b32_e32 v22, v254, v22, vcc
	v_cndmask_b32_e32 v23, v255, v23, vcc
	global_load_dword v20, v[22:23], off
	s_branch .LBB0_1196

.LBB0_1197:
	s_waitcnt vmcnt(0)
	s_or_b64 exec, exec, s[54:55]
	s_add_i32 s57, 0, 0x20800
	v_lshl_add_u32 v11, v0, 2, s57
	s_and_saveexec_b64 s[54:55], s[4:5]
	s_cbranch_execz .LBB0_1217
	ds_write_b32 v11, v1
	s_or_b64 exec, exec, s[54:55]
	s_and_saveexec_b64 s[4:5], s[6:7]
	s_cbranch_execnz .LBB0_1218

	.amdhsa_kernel _Z6mk_fwd4Args
		.amdhsa_group_segment_fixed_size 0
		.amdhsa_private_segment_fixed_size 0
		.amdhsa_kernarg_size 520
		.amdhsa_user_sgpr_count 2
		.amdhsa_user_sgpr_dispatch_ptr 0
		.amdhsa_user_sgpr_queue_ptr 0
		.amdhsa_user_sgpr_kernarg_segment_ptr 1
		.amdhsa_user_sgpr_dispatch_id 0
		.amdhsa_user_sgpr_kernarg_preload_length 0
		.amdhsa_user_sgpr_kernarg_preload_offset 0
		.amdhsa_user_sgpr_private_segment_size 0
		.amdhsa_uses_dynamic_stack 0
		.amdhsa_enable_private_segment 0
		.amdhsa_system_sgpr_workgroup_id_x 1
		.amdhsa_system_sgpr_workgroup_id_y 0
		.amdhsa_system_sgpr_workgroup_id_z 0
		.amdhsa_system_sgpr_workgroup_info 0
		.amdhsa_system_vgpr_workitem_id 0
		.amdhsa_next_free_vgpr 256
		.amdhsa_next_free_sgpr 98
		.amdhsa_accum_offset 256
		.amdhsa_reserve_vcc 1
		.amdhsa_float_round_mode_32 0
		.amdhsa_float_round_mode_16_64 0
		.amdhsa_float_denorm_mode_32 3
		.amdhsa_float_denorm_mode_16_64 3
		.amdhsa_dx10_clamp 1
		.amdhsa_ieee_mode 1
		.amdhsa_fp16_overflow 0
		.amdhsa_tg_split 0
		.amdhsa_exception_fp_ieee_invalid_op 0
		.amdhsa_exception_fp_denorm_src 0
		.amdhsa_exception_fp_ieee_div_zero 0
		.amdhsa_exception_fp_ieee_overflow 0
		.amdhsa_exception_fp_ieee_underflow 0
		.amdhsa_exception_fp_ieee_inexact 0
		.amdhsa_exception_int_div_zero 0
	.end_amdhsa_kernel

amdhsa.kernels:
  - .agpr_count:     0
    .args:
      - .offset:         0
        .size:           264
        .value_kind:     by_value
      - .offset:         264
        .size:           4
        .value_kind:     hidden_block_count_x
      - .offset:         268
        .size:           4
        .value_kind:     hidden_block_count_y
      - .offset:         272
        .size:           4
        .value_kind:     hidden_block_count_z
      - .offset:         276
        .size:           2
        .value_kind:     hidden_group_size_x
      - .offset:         278
        .size:           2
        .value_kind:     hidden_group_size_y
      - .offset:         280
        .size:           2
        .value_kind:     hidden_group_size_z
      - .offset:         282
        .size:           2
        .value_kind:     hidden_remainder_x
      - .offset:         284
        .size:           2
        .value_kind:     hidden_remainder_y
      - .offset:         286
        .size:           2
        .value_kind:     hidden_remainder_z
      - .offset:         304
        .size:           8
        .value_kind:     hidden_global_offset_x
      - .offset:         312
        .size:           8
        .value_kind:     hidden_global_offset_y
      - .offset:         320
        .size:           8
        .value_kind:     hidden_global_offset_z
      - .offset:         328
        .size:           2
        .value_kind:     hidden_grid_dims
      - .offset:         384
        .size:           4
        .value_kind:     hidden_dynamic_lds_size
    .group_segment_fixed_size: 0
    .kernarg_segment_align: 8
    .kernarg_segment_size: 520
    .language:       OpenCL C
    .language_version:
      - 2
      - 0
    .max_flat_workgroup_size: 512
    .name:           _Z6mk_fwd4Args
    .private_segment_fixed_size: 0
    .sgpr_count:     104
    .sgpr_spill_count: 134
    .symbol:         _Z6mk_fwd4Args.kd
    .uniform_work_group_size: 1
    .uses_dynamic_stack: false
    .vgpr_count:     256
    .vgpr_spill_count: 0
    .wavefront_size: 64
